# speedup vs baseline: 1.0422x; 1.0008x over previous
.Ltile0:
	s_mov_b32 s34, 0
	s_mul_i32 s35, s33, 0xa000
	v_add_u32_e32 v240, s35, v222
	v_add_u32_e32 v241, s35, v223
	v_add_u32_e32 v242, s35, v224
	s_add_u32 s33, s33, 1
	s_cmp_eq_u32 s33, 3
	s_cselect_b32 s33, 0, s33
	s_waitcnt vmcnt(5)
	s_waitcnt lgkmcnt(0)
	s_barrier
	v_mfma_scale_f32_16x16x128_f8f6f4 v[0:3], v[128:131], v[160:165], 0, v208, v216 op_sel_hi:[0,0,0] cbsz:4 blgp:2
	ds_read_b128 v[244:247], v240 offset:6144
	v_mfma_scale_f32_16x16x128_f8f6f4 v[16:19], v[132:135], v[160:165], 0, v209, v216 op_sel_hi:[0,0,0] cbsz:4 blgp:2
	ds_read_b128 v[252:255], v240 offset:7168
	v_mfma_scale_f32_16x16x128_f8f6f4 v[20:23], v[132:135], v[166:171], 0, v209, v217 op_sel_hi:[0,0,0] cbsz:4 blgp:2
	s_cmp_eq_u32 s34, 13
	s_cselect_b32 s36, s38, s36
	s_cselect_b32 s37, s39, s37
	s_mov_b32 m0, s40
	v_mfma_scale_f32_16x16x128_f8f6f4 v[4:7], v[128:131], v[166:171], 0, v208, v217 op_sel_hi:[0,0,0] cbsz:4 blgp:2
	ds_read_b128 v[184:187], v241 offset:0
	v_mfma_scale_f32_16x16x128_f8f6f4 v[8:11], v[128:131], v[172:177], 0, v208, v218 op_sel_hi:[0,0,0] cbsz:4 blgp:2
	buffer_load_dwordx4 v221, s[4:7], s36 offen lds
	v_mfma_scale_f32_16x16x128_f8f6f4 v[24:27], v[132:135], v[172:177], 0, v209, v218 op_sel_hi:[0,0,0] cbsz:4 blgp:2
	s_add_u32 m0, s40, 0x2000
	ds_read_b64 v[188:189], v242 offset:0
	v_mfma_scale_f32_16x16x128_f8f6f4 v[28:31], v[132:135], v[178:183], 0, v209, v219 op_sel_hi:[0,0,0] cbsz:4 blgp:2
	buffer_load_dwordx4 v225, s[4:7], s36 offen lds
	v_mfma_scale_f32_16x16x128_f8f6f4 v[12:15], v[128:131], v[178:183], 0, v208, v219 op_sel_hi:[0,0,0] cbsz:4 blgp:2
	s_add_u32 m0, s40, 0x4000
	ds_read_b128 v[190:193], v241 offset:1536
	v_mfma_scale_f32_16x16x128_f8f6f4 v[44:47], v[136:139], v[178:183], 0, v210, v219 op_sel_hi:[0,0,0] cbsz:4 blgp:2
	buffer_load_dwordx4 v221, s[4:7], s37 offen lds
	v_mfma_scale_f32_16x16x128_f8f6f4 v[60:63], v[140:143], v[178:183], 0, v211, v219 op_sel_hi:[0,0,0] cbsz:4 blgp:2
	s_add_u32 m0, s40, 0x6000
	ds_read_b64 v[194:195], v242 offset:1536
	v_mfma_scale_f32_16x16x128_f8f6f4 v[56:59], v[140:143], v[172:177], 0, v211, v218 op_sel_hi:[0,0,0] cbsz:4 blgp:2
	buffer_load_dwordx4 v225, s[4:7], s37 offen lds
	v_mfma_scale_f32_16x16x128_f8f6f4 v[40:43], v[136:139], v[172:177], 0, v210, v218 op_sel_hi:[0,0,0] cbsz:4 blgp:2
	s_add_u32 m0, s40, 0x8000
	ds_read_b128 v[196:199], v241 offset:3072
	v_mfma_scale_f32_16x16x128_f8f6f4 v[36:39], v[136:139], v[166:171], 0, v210, v217 op_sel_hi:[0,0,0] cbsz:4 blgp:2
	buffer_load_dwordx4 v226, s[4:7], s37 offen lds
	v_mfma_scale_f32_16x16x128_f8f6f4 v[52:55], v[140:143], v[166:171], 0, v211, v217 op_sel_hi:[0,0,0] cbsz:4 blgp:2
	ds_read_b64 v[200:201], v242 offset:3072
	v_mfma_scale_f32_16x16x128_f8f6f4 v[48:51], v[140:143], v[160:165], 0, v211, v216 op_sel_hi:[0,0,0] cbsz:4 blgp:2
	ds_read_b128 v[202:205], v241 offset:4608
	v_mfma_scale_f32_16x16x128_f8f6f4 v[32:35], v[136:139], v[160:165], 0, v210, v216 op_sel_hi:[0,0,0] cbsz:4 blgp:2
	ds_read_b64 v[206:207], v242 offset:4608
	v_mfma_scale_f32_16x16x128_f8f6f4 v[64:67], v[144:147], v[160:165], 0, v212, v216 op_sel_hi:[0,0,0] cbsz:4 blgp:2
	s_add_u32 s36, s36, 0x4000
	s_add_u32 s37, s37, 0x6000
	s_add_u32 s40, s40, 0xa000
	s_sub_u32 s41, s40, 0x1e000
	v_mfma_scale_f32_16x16x128_f8f6f4 v[80:83], v[148:151], v[160:165], 0, v213, v216 op_sel_hi:[0,0,0] cbsz:4 blgp:2
	s_cmp_ge_u32 s40, s49
	s_cselect_b32 s40, s41, s40
	ds_read_b128 v[132:135], v240 offset:1024
	v_mfma_scale_f32_16x16x128_f8f6f4 v[84:87], v[148:151], v[166:171], 0, v213, v217 op_sel_hi:[0,0,0] cbsz:4 blgp:2
	ds_read_b128 v[128:131], v240 offset:0
	v_mfma_scale_f32_16x16x128_f8f6f4 v[68:71], v[144:147], v[166:171], 0, v212, v217 op_sel_hi:[0,0,0] cbsz:4 blgp:2
	ds_read_b128 v[140:143], v240 offset:3072
	v_mfma_scale_f32_16x16x128_f8f6f4 v[72:75], v[144:147], v[172:177], 0, v212, v218 op_sel_hi:[0,0,0] cbsz:4 blgp:2
	ds_read_b128 v[136:139], v240 offset:2048
	v_mfma_scale_f32_16x16x128_f8f6f4 v[88:91], v[148:151], v[172:177], 0, v213, v218 op_sel_hi:[0,0,0] cbsz:4 blgp:2
	v_mfma_scale_f32_16x16x128_f8f6f4 v[92:95], v[148:151], v[178:183], 0, v213, v219 op_sel_hi:[0,0,0] cbsz:4 blgp:2
	v_mfma_scale_f32_16x16x128_f8f6f4 v[76:79], v[144:147], v[178:183], 0, v212, v219 op_sel_hi:[0,0,0] cbsz:4 blgp:2
	ds_read_b128 v[148:151], v240 offset:5120
	v_mfma_scale_f32_16x16x128_f8f6f4 v[108:111], v[152:155], v[178:183], 0, v214, v219 op_sel_hi:[0,0,0] cbsz:4 blgp:2
	ds_read_b128 v[144:147], v240 offset:4096
	v_mfma_scale_f32_16x16x128_f8f6f4 v[124:127], v[156:159], v[178:183], 0, v215, v219 op_sel_hi:[0,0,0] cbsz:4 blgp:2
	v_mfma_scale_f32_16x16x128_f8f6f4 v[120:123], v[156:159], v[172:177], 0, v215, v218 op_sel_hi:[0,0,0] cbsz:4 blgp:2
	v_mfma_scale_f32_16x16x128_f8f6f4 v[104:107], v[152:155], v[172:177], 0, v214, v218 op_sel_hi:[0,0,0] cbsz:4 blgp:2
	v_mfma_scale_f32_16x16x128_f8f6f4 v[100:103], v[152:155], v[166:171], 0, v214, v217 op_sel_hi:[0,0,0] cbsz:4 blgp:2
	v_mfma_scale_f32_16x16x128_f8f6f4 v[116:119], v[156:159], v[166:171], 0, v215, v217 op_sel_hi:[0,0,0] cbsz:4 blgp:2
	v_mfma_scale_f32_16x16x128_f8f6f4 v[112:115], v[156:159], v[160:165], 0, v215, v216 op_sel_hi:[0,0,0] cbsz:4 blgp:2
	v_mfma_scale_f32_16x16x128_f8f6f4 v[96:99], v[152:155], v[160:165], 0, v214, v216 op_sel_hi:[0,0,0] cbsz:4 blgp:2
	s_add_u32 s34, s34, 1
	s_mul_i32 s35, s33, 0xa000
	v_add_u32_e32 v240, s35, v222
	v_add_u32_e32 v241, s35, v223
	v_add_u32_e32 v242, s35, v224
	s_add_u32 s33, s33, 1
	s_cmp_eq_u32 s33, 3
	s_cselect_b32 s33, 0, s33
	s_waitcnt vmcnt(5)
	s_waitcnt lgkmcnt(0)
	s_barrier
	v_mfma_scale_f32_16x16x128_f8f6f4 v[0:3], v[128:131], v[184:189], v[0:3], v208, v216 op_sel_hi:[0,0,0] cbsz:4 blgp:2
	ds_read_b128 v[152:155], v240 offset:6144
	v_mfma_scale_f32_16x16x128_f8f6f4 v[16:19], v[132:135], v[184:189], v[16:19], v209, v216 op_sel_hi:[0,0,0] cbsz:4 blgp:2
	ds_read_b128 v[156:159], v240 offset:7168
	v_mfma_scale_f32_16x16x128_f8f6f4 v[20:23], v[132:135], v[190:195], v[20:23], v209, v217 op_sel_hi:[0,0,0] cbsz:4 blgp:2
	s_cmp_eq_u32 s34, 13
	s_cselect_b32 s36, s38, s36
	s_cselect_b32 s37, s39, s37
	s_mov_b32 m0, s40
	v_mfma_scale_f32_16x16x128_f8f6f4 v[4:7], v[128:131], v[190:195], v[4:7], v208, v217 op_sel_hi:[0,0,0] cbsz:4 blgp:2
	ds_read_b128 v[160:163], v241 offset:0
	v_mfma_scale_f32_16x16x128_f8f6f4 v[8:11], v[128:131], v[196:201], v[8:11], v208, v218 op_sel_hi:[0,0,0] cbsz:4 blgp:2
	buffer_load_dwordx4 v221, s[4:7], s36 offen lds
	v_mfma_scale_f32_16x16x128_f8f6f4 v[24:27], v[132:135], v[196:201], v[24:27], v209, v218 op_sel_hi:[0,0,0] cbsz:4 blgp:2
	s_add_u32 m0, s40, 0x2000
	ds_read_b64 v[164:165], v242 offset:0
	v_mfma_scale_f32_16x16x128_f8f6f4 v[28:31], v[132:135], v[202:207], v[28:31], v209, v219 op_sel_hi:[0,0,0] cbsz:4 blgp:2
	buffer_load_dwordx4 v225, s[4:7], s36 offen lds
	v_mfma_scale_f32_16x16x128_f8f6f4 v[12:15], v[128:131], v[202:207], v[12:15], v208, v219 op_sel_hi:[0,0,0] cbsz:4 blgp:2
	s_add_u32 m0, s40, 0x4000
	ds_read_b128 v[166:169], v241 offset:1536
	v_mfma_scale_f32_16x16x128_f8f6f4 v[44:47], v[136:139], v[202:207], v[44:47], v210, v219 op_sel_hi:[0,0,0] cbsz:4 blgp:2
	buffer_load_dwordx4 v221, s[4:7], s37 offen lds
	v_mfma_scale_f32_16x16x128_f8f6f4 v[60:63], v[140:143], v[202:207], v[60:63], v211, v219 op_sel_hi:[0,0,0] cbsz:4 blgp:2
	s_add_u32 m0, s40, 0x6000
	ds_read_b64 v[170:171], v242 offset:1536
	v_mfma_scale_f32_16x16x128_f8f6f4 v[56:59], v[140:143], v[196:201], v[56:59], v211, v218 op_sel_hi:[0,0,0] cbsz:4 blgp:2
	buffer_load_dwordx4 v225, s[4:7], s37 offen lds
	v_mfma_scale_f32_16x16x128_f8f6f4 v[40:43], v[136:139], v[196:201], v[40:43], v210, v218 op_sel_hi:[0,0,0] cbsz:4 blgp:2
	s_add_u32 m0, s40, 0x8000
	ds_read_b128 v[172:175], v241 offset:3072
	v_mfma_scale_f32_16x16x128_f8f6f4 v[36:39], v[136:139], v[190:195], v[36:39], v210, v217 op_sel_hi:[0,0,0] cbsz:4 blgp:2
	buffer_load_dwordx4 v226, s[4:7], s37 offen lds
	v_mfma_scale_f32_16x16x128_f8f6f4 v[52:55], v[140:143], v[190:195], v[52:55], v211, v217 op_sel_hi:[0,0,0] cbsz:4 blgp:2
	ds_read_b64 v[176:177], v242 offset:3072
	v_mfma_scale_f32_16x16x128_f8f6f4 v[48:51], v[140:143], v[184:189], v[48:51], v211, v216 op_sel_hi:[0,0,0] cbsz:4 blgp:2
	ds_read_b128 v[178:181], v241 offset:4608
	v_mfma_scale_f32_16x16x128_f8f6f4 v[32:35], v[136:139], v[184:189], v[32:35], v210, v216 op_sel_hi:[0,0,0] cbsz:4 blgp:2
	ds_read_b64 v[182:183], v242 offset:4608
	v_mfma_scale_f32_16x16x128_f8f6f4 v[64:67], v[144:147], v[184:189], v[64:67], v212, v216 op_sel_hi:[0,0,0] cbsz:4 blgp:2
	s_add_u32 s36, s36, 0x4000
	s_add_u32 s37, s37, 0x6000
	s_add_u32 s40, s40, 0xa000
	s_sub_u32 s41, s40, 0x1e000
	v_mfma_scale_f32_16x16x128_f8f6f4 v[80:83], v[148:151], v[184:189], v[80:83], v213, v216 op_sel_hi:[0,0,0] cbsz:4 blgp:2
	s_cmp_ge_u32 s40, s49
	s_cselect_b32 s40, s41, s40
	ds_read_b128 v[132:135], v240 offset:1024
	v_mfma_scale_f32_16x16x128_f8f6f4 v[84:87], v[148:151], v[190:195], v[84:87], v213, v217 op_sel_hi:[0,0,0] cbsz:4 blgp:2
	ds_read_b128 v[128:131], v240 offset:0
	v_mfma_scale_f32_16x16x128_f8f6f4 v[68:71], v[144:147], v[190:195], v[68:71], v212, v217 op_sel_hi:[0,0,0] cbsz:4 blgp:2
	ds_read_b128 v[140:143], v240 offset:3072
	v_mfma_scale_f32_16x16x128_f8f6f4 v[72:75], v[144:147], v[196:201], v[72:75], v212, v218 op_sel_hi:[0,0,0] cbsz:4 blgp:2
	ds_read_b128 v[136:139], v240 offset:2048
	v_mfma_scale_f32_16x16x128_f8f6f4 v[88:91], v[148:151], v[196:201], v[88:91], v213, v218 op_sel_hi:[0,0,0] cbsz:4 blgp:2
	v_mfma_scale_f32_16x16x128_f8f6f4 v[92:95], v[148:151], v[202:207], v[92:95], v213, v219 op_sel_hi:[0,0,0] cbsz:4 blgp:2
	v_mfma_scale_f32_16x16x128_f8f6f4 v[76:79], v[144:147], v[202:207], v[76:79], v212, v219 op_sel_hi:[0,0,0] cbsz:4 blgp:2
	ds_read_b128 v[148:151], v240 offset:5120
	v_mfma_scale_f32_16x16x128_f8f6f4 v[108:111], v[244:247], v[202:207], v[108:111], v214, v219 op_sel_hi:[0,0,0] cbsz:4 blgp:2
	ds_read_b128 v[144:147], v240 offset:4096
	v_mfma_scale_f32_16x16x128_f8f6f4 v[124:127], v[252:255], v[202:207], v[124:127], v215, v219 op_sel_hi:[0,0,0] cbsz:4 blgp:2
	v_mfma_scale_f32_16x16x128_f8f6f4 v[120:123], v[252:255], v[196:201], v[120:123], v215, v218 op_sel_hi:[0,0,0] cbsz:4 blgp:2
	v_mfma_scale_f32_16x16x128_f8f6f4 v[104:107], v[244:247], v[196:201], v[104:107], v214, v218 op_sel_hi:[0,0,0] cbsz:4 blgp:2
	v_mfma_scale_f32_16x16x128_f8f6f4 v[100:103], v[244:247], v[190:195], v[100:103], v214, v217 op_sel_hi:[0,0,0] cbsz:4 blgp:2
	v_mfma_scale_f32_16x16x128_f8f6f4 v[116:119], v[252:255], v[190:195], v[116:119], v215, v217 op_sel_hi:[0,0,0] cbsz:4 blgp:2
	v_mfma_scale_f32_16x16x128_f8f6f4 v[112:115], v[252:255], v[184:189], v[112:115], v215, v216 op_sel_hi:[0,0,0] cbsz:4 blgp:2
	v_mfma_scale_f32_16x16x128_f8f6f4 v[96:99], v[244:247], v[184:189], v[96:99], v214, v216 op_sel_hi:[0,0,0] cbsz:4 blgp:2
	s_add_u32 s34, s34, 1
.Lkloop0:
	s_mul_i32 s35, s33, 0xa000
	v_add_u32_e32 v240, s35, v222
	v_add_u32_e32 v241, s35, v223
	v_add_u32_e32 v242, s35, v224
	s_add_u32 s33, s33, 1
	s_cmp_eq_u32 s33, 3
	s_cselect_b32 s33, 0, s33
	s_waitcnt vmcnt(5)
	s_waitcnt lgkmcnt(0)
	s_barrier
	v_mfma_scale_f32_16x16x128_f8f6f4 v[0:3], v[128:131], v[160:165], v[0:3], v208, v216 op_sel_hi:[0,0,0] cbsz:4 blgp:2
	ds_read_b128 v[244:247], v240 offset:6144
	v_mfma_scale_f32_16x16x128_f8f6f4 v[16:19], v[132:135], v[160:165], v[16:19], v209, v216 op_sel_hi:[0,0,0] cbsz:4 blgp:2
	ds_read_b128 v[252:255], v240 offset:7168
	v_mfma_scale_f32_16x16x128_f8f6f4 v[20:23], v[132:135], v[166:171], v[20:23], v209, v217 op_sel_hi:[0,0,0] cbsz:4 blgp:2
	s_cmp_eq_u32 s34, 13
	s_cselect_b32 s36, s38, s36
	s_cselect_b32 s37, s39, s37
	s_mov_b32 m0, s40
	v_mfma_scale_f32_16x16x128_f8f6f4 v[4:7], v[128:131], v[166:171], v[4:7], v208, v217 op_sel_hi:[0,0,0] cbsz:4 blgp:2
	ds_read_b128 v[184:187], v241 offset:0
	v_mfma_scale_f32_16x16x128_f8f6f4 v[8:11], v[128:131], v[172:177], v[8:11], v208, v218 op_sel_hi:[0,0,0] cbsz:4 blgp:2
	buffer_load_dwordx4 v221, s[4:7], s36 offen lds
	v_mfma_scale_f32_16x16x128_f8f6f4 v[24:27], v[132:135], v[172:177], v[24:27], v209, v218 op_sel_hi:[0,0,0] cbsz:4 blgp:2
	s_add_u32 m0, s40, 0x2000
	ds_read_b64 v[188:189], v242 offset:0
	v_mfma_scale_f32_16x16x128_f8f6f4 v[28:31], v[132:135], v[178:183], v[28:31], v209, v219 op_sel_hi:[0,0,0] cbsz:4 blgp:2
	buffer_load_dwordx4 v225, s[4:7], s36 offen lds
	v_mfma_scale_f32_16x16x128_f8f6f4 v[12:15], v[128:131], v[178:183], v[12:15], v208, v219 op_sel_hi:[0,0,0] cbsz:4 blgp:2
	s_add_u32 m0, s40, 0x4000
	ds_read_b128 v[190:193], v241 offset:1536
	v_mfma_scale_f32_16x16x128_f8f6f4 v[44:47], v[136:139], v[178:183], v[44:47], v210, v219 op_sel_hi:[0,0,0] cbsz:4 blgp:2
	buffer_load_dwordx4 v221, s[4:7], s37 offen lds
	v_mfma_scale_f32_16x16x128_f8f6f4 v[60:63], v[140:143], v[178:183], v[60:63], v211, v219 op_sel_hi:[0,0,0] cbsz:4 blgp:2
	s_add_u32 m0, s40, 0x6000
	ds_read_b64 v[194:195], v242 offset:1536
	v_mfma_scale_f32_16x16x128_f8f6f4 v[56:59], v[140:143], v[172:177], v[56:59], v211, v218 op_sel_hi:[0,0,0] cbsz:4 blgp:2
	buffer_load_dwordx4 v225, s[4:7], s37 offen lds
	v_mfma_scale_f32_16x16x128_f8f6f4 v[40:43], v[136:139], v[172:177], v[40:43], v210, v218 op_sel_hi:[0,0,0] cbsz:4 blgp:2
	s_add_u32 m0, s40, 0x8000
	ds_read_b128 v[196:199], v241 offset:3072
	v_mfma_scale_f32_16x16x128_f8f6f4 v[36:39], v[136:139], v[166:171], v[36:39], v210, v217 op_sel_hi:[0,0,0] cbsz:4 blgp:2
	buffer_load_dwordx4 v226, s[4:7], s37 offen lds
	v_mfma_scale_f32_16x16x128_f8f6f4 v[52:55], v[140:143], v[166:171], v[52:55], v211, v217 op_sel_hi:[0,0,0] cbsz:4 blgp:2
	ds_read_b64 v[200:201], v242 offset:3072
	v_mfma_scale_f32_16x16x128_f8f6f4 v[48:51], v[140:143], v[160:165], v[48:51], v211, v216 op_sel_hi:[0,0,0] cbsz:4 blgp:2
	ds_read_b128 v[202:205], v241 offset:4608
	v_mfma_scale_f32_16x16x128_f8f6f4 v[32:35], v[136:139], v[160:165], v[32:35], v210, v216 op_sel_hi:[0,0,0] cbsz:4 blgp:2
	ds_read_b64 v[206:207], v242 offset:4608
	v_mfma_scale_f32_16x16x128_f8f6f4 v[64:67], v[144:147], v[160:165], v[64:67], v212, v216 op_sel_hi:[0,0,0] cbsz:4 blgp:2
	s_add_u32 s36, s36, 0x4000
	s_add_u32 s37, s37, 0x6000
	s_add_u32 s40, s40, 0xa000
	s_sub_u32 s41, s40, 0x1e000
	v_mfma_scale_f32_16x16x128_f8f6f4 v[80:83], v[148:151], v[160:165], v[80:83], v213, v216 op_sel_hi:[0,0,0] cbsz:4 blgp:2
	s_cmp_ge_u32 s40, s49
	s_cselect_b32 s40, s41, s40
	ds_read_b128 v[132:135], v240 offset:1024
	v_mfma_scale_f32_16x16x128_f8f6f4 v[84:87], v[148:151], v[166:171], v[84:87], v213, v217 op_sel_hi:[0,0,0] cbsz:4 blgp:2
	ds_read_b128 v[128:131], v240 offset:0
	v_mfma_scale_f32_16x16x128_f8f6f4 v[68:71], v[144:147], v[166:171], v[68:71], v212, v217 op_sel_hi:[0,0,0] cbsz:4 blgp:2
	ds_read_b128 v[140:143], v240 offset:3072
	v_mfma_scale_f32_16x16x128_f8f6f4 v[72:75], v[144:147], v[172:177], v[72:75], v212, v218 op_sel_hi:[0,0,0] cbsz:4 blgp:2
	ds_read_b128 v[136:139], v240 offset:2048
	v_mfma_scale_f32_16x16x128_f8f6f4 v[88:91], v[148:151], v[172:177], v[88:91], v213, v218 op_sel_hi:[0,0,0] cbsz:4 blgp:2
	v_mfma_scale_f32_16x16x128_f8f6f4 v[92:95], v[148:151], v[178:183], v[92:95], v213, v219 op_sel_hi:[0,0,0] cbsz:4 blgp:2
	v_mfma_scale_f32_16x16x128_f8f6f4 v[76:79], v[144:147], v[178:183], v[76:79], v212, v219 op_sel_hi:[0,0,0] cbsz:4 blgp:2
	ds_read_b128 v[148:151], v240 offset:5120
	v_mfma_scale_f32_16x16x128_f8f6f4 v[108:111], v[152:155], v[178:183], v[108:111], v214, v219 op_sel_hi:[0,0,0] cbsz:4 blgp:2
	ds_read_b128 v[144:147], v240 offset:4096
	v_mfma_scale_f32_16x16x128_f8f6f4 v[124:127], v[156:159], v[178:183], v[124:127], v215, v219 op_sel_hi:[0,0,0] cbsz:4 blgp:2
	v_mfma_scale_f32_16x16x128_f8f6f4 v[120:123], v[156:159], v[172:177], v[120:123], v215, v218 op_sel_hi:[0,0,0] cbsz:4 blgp:2
	v_mfma_scale_f32_16x16x128_f8f6f4 v[104:107], v[152:155], v[172:177], v[104:107], v214, v218 op_sel_hi:[0,0,0] cbsz:4 blgp:2
	v_mfma_scale_f32_16x16x128_f8f6f4 v[100:103], v[152:155], v[166:171], v[100:103], v214, v217 op_sel_hi:[0,0,0] cbsz:4 blgp:2
	v_mfma_scale_f32_16x16x128_f8f6f4 v[116:119], v[156:159], v[166:171], v[116:119], v215, v217 op_sel_hi:[0,0,0] cbsz:4 blgp:2
	v_mfma_scale_f32_16x16x128_f8f6f4 v[112:115], v[156:159], v[160:165], v[112:115], v215, v216 op_sel_hi:[0,0,0] cbsz:4 blgp:2
	v_mfma_scale_f32_16x16x128_f8f6f4 v[96:99], v[152:155], v[160:165], v[96:99], v214, v216 op_sel_hi:[0,0,0] cbsz:4 blgp:2
	s_add_u32 s34, s34, 1
	s_mul_i32 s35, s33, 0xa000
	v_add_u32_e32 v240, s35, v222
	v_add_u32_e32 v241, s35, v223
	v_add_u32_e32 v242, s35, v224
	s_add_u32 s33, s33, 1
	s_cmp_eq_u32 s33, 3
	s_cselect_b32 s33, 0, s33
	s_waitcnt vmcnt(5)
	s_waitcnt lgkmcnt(0)
	s_barrier
	v_mfma_scale_f32_16x16x128_f8f6f4 v[0:3], v[128:131], v[184:189], v[0:3], v208, v216 op_sel_hi:[0,0,0] cbsz:4 blgp:2
	ds_read_b128 v[152:155], v240 offset:6144
	v_mfma_scale_f32_16x16x128_f8f6f4 v[16:19], v[132:135], v[184:189], v[16:19], v209, v216 op_sel_hi:[0,0,0] cbsz:4 blgp:2
	ds_read_b128 v[156:159], v240 offset:7168
	v_mfma_scale_f32_16x16x128_f8f6f4 v[20:23], v[132:135], v[190:195], v[20:23], v209, v217 op_sel_hi:[0,0,0] cbsz:4 blgp:2
	s_cmp_eq_u32 s34, 13
	s_cselect_b32 s36, s38, s36
	s_cselect_b32 s37, s39, s37
	s_mov_b32 m0, s40
	v_mfma_scale_f32_16x16x128_f8f6f4 v[4:7], v[128:131], v[190:195], v[4:7], v208, v217 op_sel_hi:[0,0,0] cbsz:4 blgp:2
	ds_read_b128 v[160:163], v241 offset:0
	v_mfma_scale_f32_16x16x128_f8f6f4 v[8:11], v[128:131], v[196:201], v[8:11], v208, v218 op_sel_hi:[0,0,0] cbsz:4 blgp:2
	buffer_load_dwordx4 v221, s[4:7], s36 offen lds
	v_mfma_scale_f32_16x16x128_f8f6f4 v[24:27], v[132:135], v[196:201], v[24:27], v209, v218 op_sel_hi:[0,0,0] cbsz:4 blgp:2
	s_add_u32 m0, s40, 0x2000
	ds_read_b64 v[164:165], v242 offset:0
	v_mfma_scale_f32_16x16x128_f8f6f4 v[28:31], v[132:135], v[202:207], v[28:31], v209, v219 op_sel_hi:[0,0,0] cbsz:4 blgp:2
	buffer_load_dwordx4 v225, s[4:7], s36 offen lds
	v_mfma_scale_f32_16x16x128_f8f6f4 v[12:15], v[128:131], v[202:207], v[12:15], v208, v219 op_sel_hi:[0,0,0] cbsz:4 blgp:2
	s_add_u32 m0, s40, 0x4000
	ds_read_b128 v[166:169], v241 offset:1536
	v_mfma_scale_f32_16x16x128_f8f6f4 v[44:47], v[136:139], v[202:207], v[44:47], v210, v219 op_sel_hi:[0,0,0] cbsz:4 blgp:2
	buffer_load_dwordx4 v221, s[4:7], s37 offen lds
	v_mfma_scale_f32_16x16x128_f8f6f4 v[60:63], v[140:143], v[202:207], v[60:63], v211, v219 op_sel_hi:[0,0,0] cbsz:4 blgp:2
	s_add_u32 m0, s40, 0x6000
	ds_read_b64 v[170:171], v242 offset:1536
	v_mfma_scale_f32_16x16x128_f8f6f4 v[56:59], v[140:143], v[196:201], v[56:59], v211, v218 op_sel_hi:[0,0,0] cbsz:4 blgp:2
	buffer_load_dwordx4 v225, s[4:7], s37 offen lds
	v_mfma_scale_f32_16x16x128_f8f6f4 v[40:43], v[136:139], v[196:201], v[40:43], v210, v218 op_sel_hi:[0,0,0] cbsz:4 blgp:2
	s_add_u32 m0, s40, 0x8000
	ds_read_b128 v[172:175], v241 offset:3072
	v_mfma_scale_f32_16x16x128_f8f6f4 v[36:39], v[136:139], v[190:195], v[36:39], v210, v217 op_sel_hi:[0,0,0] cbsz:4 blgp:2
	buffer_load_dwordx4 v226, s[4:7], s37 offen lds
	v_mfma_scale_f32_16x16x128_f8f6f4 v[52:55], v[140:143], v[190:195], v[52:55], v211, v217 op_sel_hi:[0,0,0] cbsz:4 blgp:2
	ds_read_b64 v[176:177], v242 offset:3072
	v_mfma_scale_f32_16x16x128_f8f6f4 v[48:51], v[140:143], v[184:189], v[48:51], v211, v216 op_sel_hi:[0,0,0] cbsz:4 blgp:2
	ds_read_b128 v[178:181], v241 offset:4608
	v_mfma_scale_f32_16x16x128_f8f6f4 v[32:35], v[136:139], v[184:189], v[32:35], v210, v216 op_sel_hi:[0,0,0] cbsz:4 blgp:2
	ds_read_b64 v[182:183], v242 offset:4608
	v_mfma_scale_f32_16x16x128_f8f6f4 v[64:67], v[144:147], v[184:189], v[64:67], v212, v216 op_sel_hi:[0,0,0] cbsz:4 blgp:2
	s_add_u32 s36, s36, 0x4000
	s_add_u32 s37, s37, 0x6000
	s_add_u32 s40, s40, 0xa000
	s_sub_u32 s41, s40, 0x1e000
	v_mfma_scale_f32_16x16x128_f8f6f4 v[80:83], v[148:151], v[184:189], v[80:83], v213, v216 op_sel_hi:[0,0,0] cbsz:4 blgp:2
	s_cmp_ge_u32 s40, s49
	s_cselect_b32 s40, s41, s40
	ds_read_b128 v[132:135], v240 offset:1024
	v_mfma_scale_f32_16x16x128_f8f6f4 v[84:87], v[148:151], v[190:195], v[84:87], v213, v217 op_sel_hi:[0,0,0] cbsz:4 blgp:2
	ds_read_b128 v[128:131], v240 offset:0
	v_mfma_scale_f32_16x16x128_f8f6f4 v[68:71], v[144:147], v[190:195], v[68:71], v212, v217 op_sel_hi:[0,0,0] cbsz:4 blgp:2
	ds_read_b128 v[140:143], v240 offset:3072
	v_mfma_scale_f32_16x16x128_f8f6f4 v[72:75], v[144:147], v[196:201], v[72:75], v212, v218 op_sel_hi:[0,0,0] cbsz:4 blgp:2
	ds_read_b128 v[136:139], v240 offset:2048
	v_mfma_scale_f32_16x16x128_f8f6f4 v[88:91], v[148:151], v[196:201], v[88:91], v213, v218 op_sel_hi:[0,0,0] cbsz:4 blgp:2
	v_mfma_scale_f32_16x16x128_f8f6f4 v[92:95], v[148:151], v[202:207], v[92:95], v213, v219 op_sel_hi:[0,0,0] cbsz:4 blgp:2
	v_mfma_scale_f32_16x16x128_f8f6f4 v[76:79], v[144:147], v[202:207], v[76:79], v212, v219 op_sel_hi:[0,0,0] cbsz:4 blgp:2
	ds_read_b128 v[148:151], v240 offset:5120
	v_mfma_scale_f32_16x16x128_f8f6f4 v[108:111], v[244:247], v[202:207], v[108:111], v214, v219 op_sel_hi:[0,0,0] cbsz:4 blgp:2
	ds_read_b128 v[144:147], v240 offset:4096
	v_mfma_scale_f32_16x16x128_f8f6f4 v[124:127], v[252:255], v[202:207], v[124:127], v215, v219 op_sel_hi:[0,0,0] cbsz:4 blgp:2
	v_mfma_scale_f32_16x16x128_f8f6f4 v[120:123], v[252:255], v[196:201], v[120:123], v215, v218 op_sel_hi:[0,0,0] cbsz:4 blgp:2
	v_mfma_scale_f32_16x16x128_f8f6f4 v[104:107], v[244:247], v[196:201], v[104:107], v214, v218 op_sel_hi:[0,0,0] cbsz:4 blgp:2
	v_mfma_scale_f32_16x16x128_f8f6f4 v[100:103], v[244:247], v[190:195], v[100:103], v214, v217 op_sel_hi:[0,0,0] cbsz:4 blgp:2
	v_mfma_scale_f32_16x16x128_f8f6f4 v[116:119], v[252:255], v[190:195], v[116:119], v215, v217 op_sel_hi:[0,0,0] cbsz:4 blgp:2
	v_mfma_scale_f32_16x16x128_f8f6f4 v[112:115], v[252:255], v[184:189], v[112:115], v215, v216 op_sel_hi:[0,0,0] cbsz:4 blgp:2
	v_mfma_scale_f32_16x16x128_f8f6f4 v[96:99], v[244:247], v[184:189], v[96:99], v214, v216 op_sel_hi:[0,0,0] cbsz:4 blgp:2
	s_cmp_eq_u32 s34, 13
	s_cbranch_scc0 .Lnosc_or0
	s_add_u32 s44, s23, 1
	s_and_b32 s44, s44, 1
	s_cmp_lt_u32 s18, 4
	s_cselect_b32 s80, s26, s27
	s_cselect_b32 s82, s8, s10
	s_cselect_b32 s83, s9, s11
	s_lshl_b32 s80, s80, 10
	s_and_b32 s84, s18, 3
	s_lshl_b32 s84, s84, 8
	s_add_u32 s80, s80, s84
	s_add_u32 s82, s82, s80
	s_addc_u32 s83, s83, 0
	s_lshl_b32 s84, s44, 11
	s_lshl_b32 s85, s18, 8
	s_add_u32 s84, s84, s85
	s_add_u32 s84, s84, 0x1e000
	s_mov_b32 m0, s84
	v_lshlrev_b32_e32 v236, 2, v220
	global_load_lds_dword v236, s[82:83]
